# baseline (speedup 1.0000x reference)
.Lattn_prio_done:
	s_lshl_b32 s52, s13, 4
	s_lshl_b32 s0, s2, 12
	v_and_b32_e32 v56, 15, v0
	v_bfe_u32 v15, v0, 4, 2
	v_lshrrev_b32_e32 v14, 1, v0
	v_bfe_u32 v2, v0, 1, 3
	s_add_i32 s54, s52, s0
	v_lshlrev_b32_e32 v16, 7, v56
	v_bitop3_b32 v3, v15, v14, 7 bitop3:0x78
	v_bitop3_b32 v2, v15, v2, 4 bitop3:0x36
	s_bfe_u32 s53, s12, 0x50002
	v_or_b32_e32 v18, s54, v56
	v_lshl_or_b32 v57, v3, 4, v16
	v_lshl_or_b32 v81, v2, 4, v16
	v_lshl_add_u32 v2, s53, 7, v18
	v_mov_b32_e32 v3, v51
	v_lshlrev_b64 v[2:3], 7, v[2:3]
	v_and_b32_e32 v50, 48, v0
	s_waitcnt lgkmcnt(0)
	v_lshl_add_u64 v[2:3], s[14:15], 0, v[2:3]
	v_lshl_add_u64 v[12:13], v[2:3], 0, v[50:51]
	global_load_dwordx4 v[2:5], v[12:13], off offset:64 nt
	global_load_dwordx4 v[6:9], v[12:13], off nt
	v_and_b32_e32 v11, 63, v0
	v_bfe_u32 v12, v0, 5, 1
	s_mulk_i32 s13, 0xc00
	v_and_b32_e32 v13, 7, v0
	v_cmp_gt_u32_e64 s[0:1], 16, v11
	v_bitop3_b32 v11, v12, v0, 7 bitop3:0x78
	s_lshr_b32 s55, s3, 8
	s_add_i32 s3, s50, s13
	v_and_b32_e32 v14, 8, v14
	v_lshlrev_b32_e32 v23, 4, v11
	v_bitop3_b32 v11, v12, v13, 2 bitop3:0x36
	v_add3_u32 v19, s3, v16, v14
	v_bfe_u32 v14, v0, 3, 3
	v_lshlrev_b32_e32 v24, 4, v11
	v_bitop3_b32 v11, v12, v13, 4 bitop3:0x36
	v_bitop3_b32 v16, v14, v0, 7 bitop3:0x78
	v_lshlrev_b32_e32 v25, 4, v11
	v_bitop3_b32 v11, v12, v13, 6 bitop3:0x36
	v_bitop3_b32 v0, v15, v0, 15 bitop3:0x78
	v_lshl_add_u64 v[58:59], s[14:15], 0, v[50:51]
	v_lshlrev_b32_e32 v50, 4, v13
	v_lshlrev_b32_e32 v13, 4, v11
	v_or_b32_e32 v11, 8, v14
	v_lshlrev_b32_e32 v86, 4, v0
	v_bitop3_b32 v0, v15, v56, 4 bitop3:0x36
	v_or_b32_e32 v17, 4, v15
	v_lshl_add_u32 v21, v16, 4, s3
	v_lshlrev_b32_e32 v26, 7, v14
	v_lshlrev_b32_e32 v12, 6, v14
	v_lshlrev_b32_e32 v27, 7, v11
	v_lshlrev_b32_e32 v14, 6, v11
	v_lshlrev_b32_e32 v87, 4, v0
	v_or_b32_e32 v0, 8, v15
	v_bitop3_b32 v11, v15, v56, 8 bitop3:0x36
	v_bitop3_b32 v16, v15, v56, 12 bitop3:0x36
	v_lshlrev_b32_e32 v83, 2, v15
	v_add_u32_e32 v84, 0x80, v18
	v_lshl_add_u64 v[60:61], s[10:11], 0, v[50:51]
	v_lshlrev_b32_e32 v50, 4, v56
	v_lshlrev_b32_e32 v88, 4, v11
	v_or_b32_e32 v11, 12, v15
	v_lshlrev_b32_e32 v89, 4, v16
	v_lshl_add_u32 v28, v15, 8, s3
	v_lshlrev_b32_e32 v16, 6, v15
	v_lshl_add_u32 v15, v17, 8, s3
	v_lshlrev_b32_e32 v18, 6, v17
	v_lshl_add_u32 v17, v0, 8, s3
	v_lshlrev_b32_e32 v20, 6, v0
	v_add_u32_e32 v0, v1, v10
	v_lshl_add_u64 v[62:63], s[8:9], 0, v[50:51]
	s_lshl_b32 s8, s53, 1
	v_lshl_or_b32 v50, s2, 19, v0
	s_mov_b64 s[46:47], 0x2000
	v_lshl_add_u32 v85, v56, 8, s3
	v_lshl_add_u32 v29, v11, 8, s3
	v_lshlrev_b32_e32 v22, 6, v11
	s_add_i32 s3, s55, s8
	v_lshl_add_u64 v[10:11], v[50:51], 0, s[46:47]
	v_or_b32_e32 v82, s52, v56
	s_add_i32 s56, s8, 2
	s_sub_i32 s57, 0, s3
	v_lshl_add_u64 v[0:1], s[4:5], 0, v[10:11]
	s_and_b32 s78, s50, 0xc00
	s_lshl_b32 s78, s78, 1
	v_lshrrev_b32_e32 v77, 3, v65
	v_lshrrev_b32_e32 v78, 4, v65
	v_and_b32_e32 v79, 7, v65
	v_xor_b32_e32 v78, v79, v78
	v_lshlrev_b32_e32 v78, 4, v78
	v_lshl_add_u32 v77, v77, 7, v78
	v_add_u32_e32 v77, s78, v77
	v_lshl_or_b32 v64, s2, 19, v77
	v_add_u32_e32 v65, 0x400, v64
	v_xor_b32_e32 v65, 64, v65
	s_mov_b32 s58, 0x40c00000
	s_mov_b32 s36, 0x3c003c00
	v_mov_b32_e32 v116, s36
	v_mov_b32_e32 v117, s36
	v_mov_b32_e32 v118, s36
	v_mov_b32_e32 v119, s36
	v_add_u32_e32 v90, v19, v23
	v_add_u32_e32 v91, v19, v24
	v_add_u32_e32 v92, v19, v25
	v_add_u32_e32 v93, v19, v13
	v_add_u32_e32 v94, v21, v26
	v_lshlrev_b32_e32 v50, 1, v12
	v_add_u32_e32 v95, v21, v27
	v_lshlrev_b32_e32 v66, 1, v14
	v_add_u32_e32 v96, v28, v86
	v_lshlrev_b32_e32 v68, 2, v16
	v_add_u32_e32 v97, v15, v87
	v_lshlrev_b32_e32 v70, 2, v18
	v_add_u32_e32 v98, v17, v88
	v_lshlrev_b32_e32 v72, 2, v20
	v_add_u32_e32 v99, v29, v89
	v_lshlrev_b32_e32 v74, 2, v22
	v_mov_b32_e32 v100, 0xff800000
	v_mov_b32_e32 v101, 0xf149f2ca
	s_mov_b32 s59, s41
	s_branch .LBB2_3

.LBB2_22:
	s_sub_i32 s33, s33, s62
	s_cmp_lt_i32 s33, 1
	s_cselect_b64 s[2:3], -1, 0
	s_cmp_gt_i32 s33, 0
	s_cbranch_scc0 .LBB2_24
	v_add_u32_e32 v2, s60, v84
	s_mov_b32 m0, s50
	v_ashrrev_i32_e32 v3, 31, v2
	global_load_lds_dwordx4 v[52:53], off
	s_mov_b32 m0, s51
	v_lshlrev_b64 v[2:3], 7, v[2:3]
	global_load_lds_dwordx4 v[54:55], off
	v_lshl_add_u64 v[2:3], v[58:59], 0, v[2:3]
	global_load_dwordx4 v[6:9], v[2:3], off nt
	s_nop 0
	global_load_dwordx4 v[2:5], v[2:3], off offset:64 nt
